# speedup vs baseline: 1.0060x; 1.0036x over previous
.LBB3_9:
	ds_read_b128 v[146:149], v150
	ds_read_b128 v[156:159], v150 offset:2048
	ds_read_b128 v[170:173], v154
	ds_read_b128 v[174:177], v154 offset:2048
	s_mov_b32 s65, s54
	s_mov_b32 s54, s66
	ds_read_b128 v[138:141], v163
	ds_read_b128 v[126:129], v163 offset:2048
	ds_read_b128 v[142:145], v164
	ds_read_b128 v[130:133], v164 offset:2048
	ds_read_b128 v[122:125], v163 offset:4096
	ds_read_b128 v[114:117], v163 offset:6144
	ds_read_b128 v[134:137], v164 offset:4096
	ds_read_b128 v[118:121], v164 offset:6144
	s_waitcnt vmcnt(10)
	s_mul_i32 s21, s52, s22
	s_lshl_b32 s20, s27, 6
	v_add_u32_e32 v169, s65, v1
	ds_write_b128 v1, v[22:25] offset:16384
	ds_write_b128 v1, v[18:21] offset:24576
	s_nop 0
	s_add_i32 s66, s21, s20
	s_lshl_b32 s66, s66, 1
	s_add_i32 s67, s66, s51
	buffer_load_dwordx4 v[22:25], v162, s[0:3], s66 offen
	buffer_load_dwordx4 v[18:21], v162, s[0:3], s67 offen
	s_waitcnt vmcnt(10)
	ds_write_b128 v169, v[14:17] offset:32768
	ds_write_b128 v169, v[10:13] offset:40960
	s_nop 0
	s_mul_i32 s66, s53, s22
	s_add_i32 s67, s66, s20
	s_lshl_b32 s67, s67, 1
	s_add_i32 s68, s67, s51
	s_nop 4
	buffer_load_dwordx4 v[14:17], v162, s[28:31], s67 offen
	buffer_load_dwordx4 v[10:13], v162, s[28:31], s68 offen
	s_barrier
	s_waitcnt lgkmcnt(0)
	s_setprio 1
	s_waitcnt lgkmcnt(11)
	v_mfma_f32_16x16x32_f16 v[110:113], v[146:149], v[138:141], v[110:113]
	v_mfma_f32_16x16x32_f16 v[106:109], v[156:159], v[138:141], v[106:109]
	s_waitcnt lgkmcnt(10)
	v_mfma_f32_16x16x32_f16 v[102:105], v[146:149], v[126:129], v[102:105]
	v_mfma_f32_16x16x32_f16 v[98:101], v[156:159], v[126:129], v[98:101]
	s_waitcnt lgkmcnt(7)
	v_mfma_f32_16x16x32_f16 v[94:97], v[146:149], v[122:125], v[94:97]
	v_mfma_f32_16x16x32_f16 v[90:93], v[156:159], v[122:125], v[90:93]
	s_waitcnt lgkmcnt(6)
	v_mfma_f32_16x16x32_f16 v[86:89], v[146:149], v[114:117], v[86:89]
	v_mfma_f32_16x16x32_f16 v[82:85], v[156:159], v[114:117], v[82:85]
	v_mfma_f32_16x16x32_f16 v[110:113], v[170:173], v[142:145], v[110:113]
	v_mfma_f32_16x16x32_f16 v[106:109], v[174:177], v[142:145], v[106:109]
	v_mfma_f32_16x16x32_f16 v[102:105], v[170:173], v[130:133], v[102:105]
	v_mfma_f32_16x16x32_f16 v[98:101], v[174:177], v[130:133], v[98:101]
	s_waitcnt lgkmcnt(5)
	v_mfma_f32_16x16x32_f16 v[94:97], v[170:173], v[134:137], v[94:97]
	v_mfma_f32_16x16x32_f16 v[90:93], v[174:177], v[134:137], v[90:93]
	s_waitcnt lgkmcnt(4)
	v_mfma_f32_16x16x32_f16 v[86:89], v[170:173], v[118:121], v[86:89]
	v_mfma_f32_16x16x32_f16 v[82:85], v[174:177], v[118:121], v[82:85]
	s_setprio 0
	s_barrier
	ds_read_b128 v[146:149], v150 offset:16384
	ds_read_b128 v[150:153], v150 offset:18432
	ds_read_b128 v[158:161], v154 offset:16384
	ds_read_b128 v[154:157], v154 offset:18432
	s_waitcnt vmcnt(10)
	s_add_i32 s67, s66, s51
	s_add_i32 s20, s67, s20
	s_lshl_b32 s20, s20, 1
	ds_write_b128 v169, v[6:9] offset:49152
	ds_write_b128 v169, v[2:5] offset:57344
	s_add_i32 s68, s20, s51
	s_nop 4
	buffer_load_dwordx4 v[6:9], v162, s[28:31], s20 offen
	buffer_load_dwordx4 v[2:5], v162, s[28:31], s68 offen
	s_add_i32 s27, s27, 1
	s_cmp_eq_u32 s27, s55
	s_cbranch_scc0 .LBB3_13
	s_add_i32 s20, s64, 1
	s_cmp_gt_i32 s64, -1
	s_cbranch_scc1 .LBB3_12
	s_mul_i32 s0, s20, s33
	s_add_i32 s0, s0, s44
	s_abs_i32 s21, s0
	s_mul_hi_u32 s27, s21, s46
	s_mul_i32 s28, s27, s43
	s_ashr_i32 s1, s0, 31
	s_sub_i32 s21, s21, s28
	s_xor_b32 s1, s1, s45
	s_add_i32 s28, s27, 1
	s_sub_i32 s29, s21, s43
	s_cmp_ge_u32 s21, s43
	s_cselect_b32 s27, s28, s27
	s_cselect_b32 s21, s29, s21
	s_add_i32 s28, s27, 1
	s_cmp_ge_u32 s21, s43
	s_cselect_b32 s21, s28, s27
	s_xor_b32 s21, s21, s1
	s_sub_i32 s1, s21, s1
	s_mul_i32 s21, s1, s42
	s_sub_i32 s0, s0, s21
	s_abs_i32 s27, s0
	s_mul_hi_u32 s28, s27, s49
	s_mul_i32 s29, s28, s47
	s_ashr_i32 s21, s0, 31
	s_sub_i32 s27, s27, s29
	s_xor_b32 s21, s21, s48
	s_add_i32 s29, s28, 1
	s_sub_i32 s30, s27, s47
	s_cmp_ge_u32 s27, s47
	s_cselect_b32 s28, s29, s28
	s_cselect_b32 s27, s30, s27
	s_add_i32 s29, s28, 1
	s_cmp_ge_u32 s27, s47
	s_cselect_b32 s27, s29, s28
	s_xor_b32 s27, s27, s21
	s_sub_i32 s21, s27, s21
	s_lshl_b32 s52, s21, 7
	s_mul_i32 s21, s21, s23
	s_sub_i32 s0, s0, s21
	s_lshl_b32 s53, s0, 8
	s_cmp_eq_u32 s1, 1
	s_cselect_b32 s21, s7, s9
	s_cselect_b32 s0, s6, s8
	s_cselect_b32 s27, s13, s15
	s_cselect_b32 s28, s12, s14
	s_cmp_eq_u32 s1, 0
	s_cselect_b32 s1, s5, s21
	s_cselect_b32 s21, s11, s27
	s_mov_b32 s27, s3
	s_mul_i32 s66, s53, s22
	s_cselect_b32 s0, s4, s0
	s_cselect_b32 s28, s10, s28
	s_and_b32 s1, s1, 0xffff
	s_and_b32 s29, s21, 0xffff
	s_mul_i32 s21, s52, s22
	s_add_i32 s67, s66, s51
	s_mov_b64 s[30:31], s[26:27]

.LBB3_14:
	s_barrier
	s_waitcnt lgkmcnt(0)
	s_setprio 1
	s_waitcnt lgkmcnt(5)
	v_mfma_f32_16x16x32_f16 v[78:81], v[146:149], v[138:141], v[78:81]
	s_waitcnt lgkmcnt(4)
	v_mfma_f32_16x16x32_f16 v[74:77], v[150:153], v[138:141], v[74:77]
	v_mfma_f32_16x16x32_f16 v[70:73], v[146:149], v[126:129], v[70:73]
	v_mfma_f32_16x16x32_f16 v[66:69], v[150:153], v[126:129], v[66:69]
	v_mfma_f32_16x16x32_f16 v[62:65], v[146:149], v[122:125], v[62:65]
	v_mfma_f32_16x16x32_f16 v[58:61], v[150:153], v[122:125], v[58:61]
	v_mfma_f32_16x16x32_f16 v[54:57], v[146:149], v[114:117], v[54:57]
	v_mfma_f32_16x16x32_f16 v[50:53], v[150:153], v[114:117], v[50:53]
	s_waitcnt lgkmcnt(3)
	v_mfma_f32_16x16x32_f16 v[78:81], v[158:161], v[142:145], v[78:81]
	s_waitcnt lgkmcnt(2)
	v_mfma_f32_16x16x32_f16 v[74:77], v[154:157], v[142:145], v[74:77]
	v_mfma_f32_16x16x32_f16 v[70:73], v[158:161], v[130:133], v[70:73]
	v_mfma_f32_16x16x32_f16 v[66:69], v[154:157], v[130:133], v[66:69]
	v_mfma_f32_16x16x32_f16 v[62:65], v[158:161], v[134:137], v[62:65]
	v_mfma_f32_16x16x32_f16 v[58:61], v[154:157], v[134:137], v[58:61]
	v_mfma_f32_16x16x32_f16 v[54:57], v[158:161], v[118:121], v[54:57]
	v_mfma_f32_16x16x32_f16 v[50:53], v[154:157], v[118:121], v[50:53]
	s_setprio 0
	s_barrier
	v_add_u32_e32 v169, s65, v165
	v_add_u32_e32 v170, s65, v168
	ds_read_b128 v[146:149], v169 offset:32768
	ds_read_b128 v[150:153], v169 offset:34816
	ds_read_b128 v[154:157], v170 offset:32768
	ds_read_b128 v[158:161], v170 offset:34816
	ds_read_b128 v[138:141], v163 offset:16384
	ds_read_b128 v[126:129], v163 offset:18432
	ds_read_b128 v[142:145], v164 offset:16384
	ds_read_b128 v[130:133], v164 offset:18432
	ds_read_b128 v[122:125], v163 offset:20480
	ds_read_b128 v[114:117], v163 offset:22528
	ds_read_b128 v[134:137], v164 offset:20480
	ds_read_b128 v[118:121], v164 offset:22528
	s_waitcnt vmcnt(10)
	s_lshl_b32 s64, s27, 6
	v_add_u32_e32 v171, s62, v1
	s_add_i32 s21, s21, s64
	ds_write_b128 v1, v[46:49]
	ds_write_b128 v1, v[42:45] offset:8192
	s_nop 0
	s_lshl_b32 s21, s21, 1
	s_add_i32 s68, s21, s51
	buffer_load_dwordx4 v[46:49], v162, s[0:3], s21 offen
	buffer_load_dwordx4 v[42:45], v162, s[0:3], s68 offen
	s_waitcnt vmcnt(10)
	ds_write_b128 v171, v[38:41] offset:32768
	ds_write_b128 v171, v[34:37] offset:40960
	s_nop 0
	s_add_i32 s21, s66, s64
	s_lshl_b32 s21, s21, 1
	s_add_i32 s66, s21, s51
	s_nop 4
	buffer_load_dwordx4 v[38:41], v162, s[28:31], s21 offen
	buffer_load_dwordx4 v[34:37], v162, s[28:31], s66 offen
	s_barrier
	s_waitcnt lgkmcnt(0)
	s_setprio 1
	s_waitcnt lgkmcnt(11)
	v_mfma_f32_16x16x32_f16 v[110:113], v[146:149], v[138:141], v[110:113]
	v_mfma_f32_16x16x32_f16 v[106:109], v[150:153], v[138:141], v[106:109]
	s_waitcnt lgkmcnt(10)
	v_mfma_f32_16x16x32_f16 v[102:105], v[146:149], v[126:129], v[102:105]
	v_mfma_f32_16x16x32_f16 v[98:101], v[150:153], v[126:129], v[98:101]
	s_waitcnt lgkmcnt(7)
	v_mfma_f32_16x16x32_f16 v[94:97], v[146:149], v[122:125], v[94:97]
	v_mfma_f32_16x16x32_f16 v[90:93], v[150:153], v[122:125], v[90:93]
	s_waitcnt lgkmcnt(6)
	v_mfma_f32_16x16x32_f16 v[86:89], v[146:149], v[114:117], v[86:89]
	v_mfma_f32_16x16x32_f16 v[82:85], v[150:153], v[114:117], v[82:85]
	v_mfma_f32_16x16x32_f16 v[110:113], v[154:157], v[142:145], v[110:113]
	v_mfma_f32_16x16x32_f16 v[106:109], v[158:161], v[142:145], v[106:109]
	v_mfma_f32_16x16x32_f16 v[102:105], v[154:157], v[130:133], v[102:105]
	v_mfma_f32_16x16x32_f16 v[98:101], v[158:161], v[130:133], v[98:101]
	s_waitcnt lgkmcnt(5)
	v_mfma_f32_16x16x32_f16 v[94:97], v[154:157], v[134:137], v[94:97]
	v_mfma_f32_16x16x32_f16 v[90:93], v[158:161], v[134:137], v[90:93]
	s_waitcnt lgkmcnt(4)
	v_mfma_f32_16x16x32_f16 v[86:89], v[154:157], v[118:121], v[86:89]
	v_mfma_f32_16x16x32_f16 v[82:85], v[158:161], v[118:121], v[82:85]
	s_setprio 0
	s_barrier
	ds_read_b128 v[146:149], v169 offset:49152
	ds_read_b128 v[150:153], v169 offset:51200
	ds_read_b128 v[158:161], v170 offset:49152
	ds_read_b128 v[154:157], v170 offset:51200
	s_waitcnt vmcnt(10)
	s_add_i32 s21, s67, s64
	s_lshl_b32 s21, s21, 1
	s_add_i32 s64, s21, s51
	ds_write_b128 v171, v[30:33] offset:49152
	ds_write_b128 v171, v[26:29] offset:57344
	s_nop 4
	buffer_load_dwordx4 v[30:33], v162, s[28:31], s21 offen
	buffer_load_dwordx4 v[26:29], v162, s[28:31], s64 offen
	s_add_i32 s27, s27, 1
	s_cmp_lg_u32 s27, s55
	s_cbranch_scc1 .LBB3_18
	s_add_i32 s64, s20, 1
	s_cmp_gt_i32 s20, -1
	s_cbranch_scc1 .LBB3_17
	s_mul_i32 s0, s64, s33
	s_add_i32 s0, s0, s44
	s_abs_i32 s20, s0
	s_mul_hi_u32 s21, s20, s46
	s_mul_i32 s27, s21, s43
	s_ashr_i32 s1, s0, 31
	s_sub_i32 s20, s20, s27
	s_xor_b32 s1, s1, s45
	s_add_i32 s27, s21, 1
	s_sub_i32 s28, s20, s43
	s_cmp_ge_u32 s20, s43
	s_cselect_b32 s21, s27, s21
	s_cselect_b32 s20, s28, s20
	s_add_i32 s27, s21, 1
	s_cmp_ge_u32 s20, s43
	s_cselect_b32 s20, s27, s21
	s_xor_b32 s20, s20, s1
	s_sub_i32 s1, s20, s1
	s_mul_i32 s20, s1, s42
	s_sub_i32 s0, s0, s20
	s_abs_i32 s21, s0
	s_mul_hi_u32 s27, s21, s49
	s_mul_i32 s28, s27, s47
	s_ashr_i32 s20, s0, 31
	s_sub_i32 s21, s21, s28
	s_xor_b32 s20, s20, s48
	s_add_i32 s28, s27, 1
	s_sub_i32 s29, s21, s47
	s_cmp_ge_u32 s21, s47
	s_cselect_b32 s27, s28, s27
	s_cselect_b32 s21, s29, s21
	s_add_i32 s28, s27, 1
	s_cmp_ge_u32 s21, s47
	s_cselect_b32 s21, s28, s27
	s_xor_b32 s21, s21, s20
	s_sub_i32 s20, s21, s20
	s_lshl_b32 s52, s20, 7
	s_mul_i32 s20, s20, s23
	s_sub_i32 s0, s0, s20
	s_lshl_b32 s53, s0, 8
	s_cmp_eq_u32 s1, 1
	s_cselect_b32 s20, s7, s9
	s_cselect_b32 s0, s6, s8
	s_cselect_b32 s21, s13, s15
	s_cselect_b32 s27, s12, s14
	s_cmp_eq_u32 s1, 0
	s_cselect_b32 s1, s5, s20
	s_cselect_b32 s28, s10, s27
	s_cselect_b32 s20, s11, s21
	s_mov_b32 s27, s3
	s_cselect_b32 s0, s4, s0
	s_and_b32 s1, s1, 0xffff
	s_and_b32 s29, s20, 0xffff
	s_mov_b64 s[30:31], s[26:27]
